# grid barrier: all workgroups poll the cross-XCC release word directly (one hop less)
# speedup vs baseline: 1.0127x; 1.0006x over previous
; __device__ __forceinline__ unsigned xb_ld(unsigned* p)              { return __hip_atomic_load(p, __ATOMIC_RELAXED, __HIP_MEMORY_SCOPE_AGENT); }
; __device__ __forceinline__ unsigned xb_add(unsigned* p, unsigned v) { return __hip_atomic_fetch_add(p, v, __ATOMIC_RELAXED, __HIP_MEMORY_SCOPE_AGENT); }
; #define XB_SPIN(cond, bar) do { unsigned _sp = 0; while (cond) { __builtin_amdgcn_s_sleep(1); \
;     if ((++_sp & 255u) == 0u) { if (xb_ld(&(bar)[XB_TMO])) break; if (_sp > XB_SPIN_CAP) { atomicAdd(&(bar)[XB_TMO], 1u); break; } } } } while (0)
; __device__ __forceinline__ void xcd_barrier(const XcdBarrier& b, bool t0) {
;     ...
;         const unsigned old = xb_add(&bar[XB_XSUB(b.x)], 1u);
;         const unsigned gen = old / nloc;
;         if (old + 1u == (gen + 1u) * nloc) {
;             __builtin_amdgcn_fence(__ATOMIC_RELEASE, "agent");
;             asm volatile("s_waitcnt vmcnt(0)" ::: "memory");
;             const unsigned og = xb_add(&bar[XB_TOP], 1u);
;             const unsigned tg = og / nx;
;             if (og + 1u == (tg + 1u) * nx) xb_add(&bar[XB_TOPGEN], 1u);
;             else XB_SPIN(xb_ld(&bar[XB_TOPGEN]) == tg, bar);
;             __builtin_amdgcn_fence(__ATOMIC_ACQUIRE, "agent");
;             xb_add(&bar[XB_XGEN(b.x)], 1u);
;             asm volatile("s_waitcnt vmcnt(0)" ::: "memory");
;         } else {
;             XB_SPIN(xb_ld(&bar[XB_XGEN(b.x)]) == gen, bar);
;             __builtin_amdgcn_fence(__ATOMIC_ACQUIRE, "agent");
.LBB0_214:
	v_readlane_b32 s3, v254, 45
	s_lshl_b32 s3, s3, 8
	v_readlane_b32 s6, v254, 43
	v_readlane_b32 s7, v254, 44
	s_add_u32 s6, s6, s3
	s_addc_u32 s7, s7, 0
	v_mov_b32_e32 v1, 0x1000
	v_mov_b32_e32 v3, 1
	v_sub_u32_e32 v4, 0, v2
	global_atomic_add v3, v1, v3, s[6:7] offset:1024 sc0
	v_cvt_f32_u32_e32 v1, v2
	v_rcp_iflag_f32_e32 v1, v1
	s_nop 0
	v_mul_f32_e32 v1, 0x4f7ffffe, v1
	v_cvt_u32_f32_e32 v1, v1
	v_mul_lo_u32 v4, v4, v1
	v_mul_hi_u32 v4, v1, v4
	v_add_u32_e32 v1, v1, v4
	s_waitcnt vmcnt(0)
	v_mul_hi_u32 v1, v3, v1
	v_mul_lo_u32 v4, v1, v2
	v_sub_u32_e32 v4, v3, v4
	v_add_u32_e32 v5, 1, v1
	v_cmp_ge_u32_e32 vcc, v4, v2
	v_add_u32_e32 v3, 1, v3
	s_nop 0
	v_cndmask_b32_e32 v1, v1, v5, vcc
	v_sub_u32_e32 v5, v4, v2
	v_cndmask_b32_e32 v4, v4, v5, vcc
	v_add_u32_e32 v5, 1, v1
	v_cmp_ge_u32_e32 vcc, v4, v2
	s_nop 1
	v_cndmask_b32_e32 v1, v1, v5, vcc
	v_mul_lo_u32 v4, v2, v1
	v_add_u32_e32 v2, v4, v2
	v_cmp_ne_u32_e32 vcc, v3, v2
	s_and_saveexec_b64 s[8:9], vcc
	s_xor_b64 s[8:9], exec, s[8:9]
	s_cbranch_execz .LBB0_228
	s_waitcnt lgkmcnt(0)
	v_mov_b32_e32 v0, 0x7500
	global_load_dword v0, v0, s[46:47] sc1
	s_add_u32 s14, s46, 0x7500
	s_addc_u32 s15, s47, 0
	s_waitcnt vmcnt(0)
	v_cmp_eq_u32_e32 vcc, v0, v1
	s_and_saveexec_b64 s[10:11], vcc
	s_cbranch_execz .LBB0_227
	s_add_u32 s12, s46, 0x4200
	s_addc_u32 s13, s47, 0
	s_mov_b32 s3, 1
	s_mov_b64 s[16:17], 0
	v_mov_b32_e32 v0, 0
	s_branch .LBB0_218

; __device__ __forceinline__ unsigned xb_ld(unsigned* p)              { return __hip_atomic_load(p, __ATOMIC_RELAXED, __HIP_MEMORY_SCOPE_AGENT); }
; __device__ __forceinline__ unsigned xb_add(unsigned* p, unsigned v) { return __hip_atomic_fetch_add(p, v, __ATOMIC_RELAXED, __HIP_MEMORY_SCOPE_AGENT); }
; #define XB_SPIN(cond, bar) do { unsigned _sp = 0; while (cond) { __builtin_amdgcn_s_sleep(1); \
;     if ((++_sp & 255u) == 0u) { if (xb_ld(&(bar)[XB_TMO])) break; if (_sp > XB_SPIN_CAP) { atomicAdd(&(bar)[XB_TMO], 1u); break; } } } } while (0)
; __device__ __forceinline__ void xcd_barrier(const XcdBarrier& b, bool t0) {
;     ...
;         const unsigned old = xb_add(&bar[XB_XSUB(b.x)], 1u);
;         const unsigned gen = old / nloc;
;         if (old + 1u == (gen + 1u) * nloc) {
;             __builtin_amdgcn_fence(__ATOMIC_RELEASE, "agent");
;             asm volatile("s_waitcnt vmcnt(0)" ::: "memory");
;             const unsigned og = xb_add(&bar[XB_TOP], 1u);
;             const unsigned tg = og / nx;
;             if (og + 1u == (tg + 1u) * nx) xb_add(&bar[XB_TOPGEN], 1u);
;             else XB_SPIN(xb_ld(&bar[XB_TOPGEN]) == tg, bar);
;             __builtin_amdgcn_fence(__ATOMIC_ACQUIRE, "agent");
;             xb_add(&bar[XB_XGEN(b.x)], 1u);
;             asm volatile("s_waitcnt vmcnt(0)" ::: "memory");
;         } else {
;             XB_SPIN(xb_ld(&bar[XB_XGEN(b.x)]) == gen, bar);
;             __builtin_amdgcn_fence(__ATOMIC_ACQUIRE, "agent");
.LBB0_479:
	v_readlane_b32 s3, v254, 45
	s_lshl_b32 s3, s3, 8
	v_readlane_b32 s6, v254, 43
	v_readlane_b32 s7, v254, 44
	s_add_u32 s6, s6, s3
	s_addc_u32 s7, s7, 0
	v_mov_b32_e32 v1, 0x1000
	v_mov_b32_e32 v4, 1
	v_sub_u32_e32 v5, 0, v3
	global_atomic_add v4, v1, v4, s[6:7] offset:1024 sc0
	v_cvt_f32_u32_e32 v1, v3
	v_rcp_iflag_f32_e32 v1, v1
	s_nop 0
	v_mul_f32_e32 v1, 0x4f7ffffe, v1
	v_cvt_u32_f32_e32 v1, v1
	v_mul_lo_u32 v5, v5, v1
	v_mul_hi_u32 v5, v1, v5
	v_add_u32_e32 v1, v1, v5
	s_waitcnt vmcnt(0)
	v_mul_hi_u32 v1, v4, v1
	v_mul_lo_u32 v5, v1, v3
	v_sub_u32_e32 v5, v4, v5
	v_add_u32_e32 v6, 1, v1
	v_cmp_ge_u32_e32 vcc, v5, v3
	v_add_u32_e32 v4, 1, v4
	s_nop 0
	v_cndmask_b32_e32 v1, v1, v6, vcc
	v_sub_u32_e32 v6, v5, v3
	v_cndmask_b32_e32 v5, v5, v6, vcc
	v_add_u32_e32 v6, 1, v1
	v_cmp_ge_u32_e32 vcc, v5, v3
	s_nop 1
	v_cndmask_b32_e32 v1, v1, v6, vcc
	v_mul_lo_u32 v5, v3, v1
	v_add_u32_e32 v3, v5, v3
	v_cmp_ne_u32_e32 vcc, v4, v3
	s_and_saveexec_b64 s[8:9], vcc
	s_xor_b64 s[8:9], exec, s[8:9]
	s_cbranch_execz .LBB0_493
	s_waitcnt lgkmcnt(0)
	v_mov_b32_e32 v0, 0x7500
	global_load_dword v0, v0, s[46:47] sc1
	s_add_u32 s14, s46, 0x7500
	s_addc_u32 s15, s47, 0
	s_waitcnt vmcnt(0)
	v_cmp_eq_u32_e32 vcc, v0, v1
	s_and_saveexec_b64 s[10:11], vcc
	s_cbranch_execz .LBB0_492
	s_add_u32 s12, s46, 0x4200
	s_addc_u32 s13, s47, 0
	s_mov_b32 s3, 1
	s_mov_b64 s[16:17], 0
	v_mov_b32_e32 v0, 0
	s_branch .LBB0_483

; __device__ __forceinline__ unsigned xb_ld(unsigned* p)              { return __hip_atomic_load(p, __ATOMIC_RELAXED, __HIP_MEMORY_SCOPE_AGENT); }
; __device__ __forceinline__ unsigned xb_add(unsigned* p, unsigned v) { return __hip_atomic_fetch_add(p, v, __ATOMIC_RELAXED, __HIP_MEMORY_SCOPE_AGENT); }
; #define XB_SPIN(cond, bar) do { unsigned _sp = 0; while (cond) { __builtin_amdgcn_s_sleep(1); \
;     if ((++_sp & 255u) == 0u) { if (xb_ld(&(bar)[XB_TMO])) break; if (_sp > XB_SPIN_CAP) { atomicAdd(&(bar)[XB_TMO], 1u); break; } } } } while (0)
; __device__ __forceinline__ void xcd_barrier(const XcdBarrier& b, bool t0) {
;     ...
;         const unsigned old = xb_add(&bar[XB_XSUB(b.x)], 1u);
;         const unsigned gen = old / nloc;
;         if (old + 1u == (gen + 1u) * nloc) {
;             __builtin_amdgcn_fence(__ATOMIC_RELEASE, "agent");
;             asm volatile("s_waitcnt vmcnt(0)" ::: "memory");
;             const unsigned og = xb_add(&bar[XB_TOP], 1u);
;             const unsigned tg = og / nx;
;             if (og + 1u == (tg + 1u) * nx) xb_add(&bar[XB_TOPGEN], 1u);
;             else XB_SPIN(xb_ld(&bar[XB_TOPGEN]) == tg, bar);
;             __builtin_amdgcn_fence(__ATOMIC_ACQUIRE, "agent");
;             xb_add(&bar[XB_XGEN(b.x)], 1u);
;             asm volatile("s_waitcnt vmcnt(0)" ::: "memory");
;         } else {
;             XB_SPIN(xb_ld(&bar[XB_XGEN(b.x)]) == gen, bar);
;             __builtin_amdgcn_fence(__ATOMIC_ACQUIRE, "agent");
.LBB0_534:
	v_readlane_b32 s3, v254, 45
	s_lshl_b32 s3, s3, 8
	v_readlane_b32 s6, v254, 43
	v_readlane_b32 s7, v254, 44
	s_add_u32 s6, s6, s3
	s_addc_u32 s7, s7, 0
	v_mov_b32_e32 v1, 0x1000
	v_mov_b32_e32 v5, 1
	v_sub_u32_e32 v6, 0, v4
	global_atomic_add v5, v1, v5, s[6:7] offset:1024 sc0
	v_cvt_f32_u32_e32 v1, v4
	v_rcp_iflag_f32_e32 v1, v1
	s_nop 0
	v_mul_f32_e32 v1, 0x4f7ffffe, v1
	v_cvt_u32_f32_e32 v1, v1
	v_mul_lo_u32 v6, v6, v1
	v_mul_hi_u32 v6, v1, v6
	v_add_u32_e32 v1, v1, v6
	s_waitcnt vmcnt(0)
	v_mul_hi_u32 v1, v5, v1
	v_mul_lo_u32 v6, v1, v4
	v_sub_u32_e32 v6, v5, v6
	v_add_u32_e32 v7, 1, v1
	v_cmp_ge_u32_e32 vcc, v6, v4
	v_add_u32_e32 v5, 1, v5
	s_nop 0
	v_cndmask_b32_e32 v1, v1, v7, vcc
	v_sub_u32_e32 v7, v6, v4
	v_cndmask_b32_e32 v6, v6, v7, vcc
	v_add_u32_e32 v7, 1, v1
	v_cmp_ge_u32_e32 vcc, v6, v4
	s_nop 1
	v_cndmask_b32_e32 v1, v1, v7, vcc
	v_mul_lo_u32 v6, v4, v1
	v_add_u32_e32 v4, v6, v4
	v_cmp_ne_u32_e32 vcc, v5, v4
	s_and_saveexec_b64 s[8:9], vcc
	s_xor_b64 s[8:9], exec, s[8:9]
	s_cbranch_execz .LBB0_548
	s_waitcnt lgkmcnt(0)
	v_mov_b32_e32 v0, 0x7500
	global_load_dword v0, v0, s[46:47] sc1
	s_add_u32 s14, s46, 0x7500
	s_addc_u32 s15, s47, 0
	s_waitcnt vmcnt(0)
	v_cmp_eq_u32_e32 vcc, v0, v1
	s_and_saveexec_b64 s[10:11], vcc
	s_cbranch_execz .LBB0_547
	s_add_u32 s12, s46, 0x4200
	s_addc_u32 s13, s47, 0
	s_mov_b32 s3, 1
	s_mov_b64 s[16:17], 0
	v_mov_b32_e32 v0, 0
	s_branch .LBB0_538

; __device__ __forceinline__ unsigned xb_ld(unsigned* p)              { return __hip_atomic_load(p, __ATOMIC_RELAXED, __HIP_MEMORY_SCOPE_AGENT); }
; __device__ __forceinline__ unsigned xb_add(unsigned* p, unsigned v) { return __hip_atomic_fetch_add(p, v, __ATOMIC_RELAXED, __HIP_MEMORY_SCOPE_AGENT); }
; #define XB_SPIN(cond, bar) do { unsigned _sp = 0; while (cond) { __builtin_amdgcn_s_sleep(1); \
;     if ((++_sp & 255u) == 0u) { if (xb_ld(&(bar)[XB_TMO])) break; if (_sp > XB_SPIN_CAP) { atomicAdd(&(bar)[XB_TMO], 1u); break; } } } } while (0)
; __device__ __forceinline__ void xcd_barrier(const XcdBarrier& b, bool t0) {
;     ...
;         const unsigned old = xb_add(&bar[XB_XSUB(b.x)], 1u);
;         const unsigned gen = old / nloc;
;         if (old + 1u == (gen + 1u) * nloc) {
;             __builtin_amdgcn_fence(__ATOMIC_RELEASE, "agent");
;             asm volatile("s_waitcnt vmcnt(0)" ::: "memory");
;             const unsigned og = xb_add(&bar[XB_TOP], 1u);
;             const unsigned tg = og / nx;
;             if (og + 1u == (tg + 1u) * nx) xb_add(&bar[XB_TOPGEN], 1u);
;             else XB_SPIN(xb_ld(&bar[XB_TOPGEN]) == tg, bar);
;             __builtin_amdgcn_fence(__ATOMIC_ACQUIRE, "agent");
;             xb_add(&bar[XB_XGEN(b.x)], 1u);
;             asm volatile("s_waitcnt vmcnt(0)" ::: "memory");
;         } else {
;             XB_SPIN(xb_ld(&bar[XB_XGEN(b.x)]) == gen, bar);
;             __builtin_amdgcn_fence(__ATOMIC_ACQUIRE, "agent");
.LBB0_1646:
	v_readlane_b32 s3, v254, 45
	s_lshl_b32 s3, s3, 8
	v_readlane_b32 s4, v254, 43
	v_readlane_b32 s5, v254, 44
	s_add_u32 s4, s4, s3
	s_addc_u32 s5, s5, 0
	v_mov_b32_e32 v1, 0x1000
	v_mov_b32_e32 v3, 1
	v_sub_u32_e32 v4, 0, v2
	global_atomic_add v3, v1, v3, s[4:5] offset:1024 sc0
	v_cvt_f32_u32_e32 v1, v2
	v_rcp_iflag_f32_e32 v1, v1
	s_nop 0
	v_mul_f32_e32 v1, 0x4f7ffffe, v1
	v_cvt_u32_f32_e32 v1, v1
	v_mul_lo_u32 v4, v4, v1
	v_mul_hi_u32 v4, v1, v4
	v_add_u32_e32 v1, v1, v4
	s_waitcnt vmcnt(0)
	v_mul_hi_u32 v1, v3, v1
	v_mul_lo_u32 v4, v1, v2
	v_sub_u32_e32 v4, v3, v4
	v_add_u32_e32 v5, 1, v1
	v_cmp_ge_u32_e32 vcc, v4, v2
	v_add_u32_e32 v3, 1, v3
	s_nop 0
	v_cndmask_b32_e32 v1, v1, v5, vcc
	v_sub_u32_e32 v5, v4, v2
	v_cndmask_b32_e32 v4, v4, v5, vcc
	v_add_u32_e32 v5, 1, v1
	v_cmp_ge_u32_e32 vcc, v4, v2
	s_nop 1
	v_cndmask_b32_e32 v1, v1, v5, vcc
	v_mul_lo_u32 v4, v2, v1
	v_add_u32_e32 v2, v4, v2
	v_cmp_ne_u32_e32 vcc, v3, v2
	s_and_saveexec_b64 s[6:7], vcc
	s_xor_b64 s[6:7], exec, s[6:7]
	s_cbranch_execz .LBB0_1660
	s_waitcnt lgkmcnt(0)
	v_mov_b32_e32 v0, 0x7500
	global_load_dword v0, v0, s[46:47] sc1
	s_add_u32 s12, s46, 0x7500
	s_addc_u32 s13, s47, 0
	s_waitcnt vmcnt(0)
	v_cmp_eq_u32_e32 vcc, v0, v1
	s_and_saveexec_b64 s[8:9], vcc
	s_cbranch_execz .LBB0_1659
	s_add_u32 s10, s46, 0x4200
	s_addc_u32 s11, s47, 0
	s_mov_b32 s3, 1
	s_mov_b64 s[14:15], 0
	v_mov_b32_e32 v0, 0
	s_branch .LBB0_1650
